# MoBA unit set-up: row-table scan branch-free over the running prefix (one batch of LDS reads instead of up to 30 dependent ones)
# baseline (speedup 1.0000x reference)
; __device__ __forceinline__ void moba_unit(const UnitRef& u, char* lds, int* rowtab, int* cq, float* wscr, int* idx_slot, const int pend_idx, const int wid) {
;     ...
;         const int sidx = u.c * 512 + tid; int ent = -1;
;         if (sidx < 256) ent = (u.n * 256 + sidx) | (3 << 16);
;         else { const int g = sidx - 256;
;             if (g < u.L) { int acc = 0, qx = u.n + 1;
;                 while (qx < 31 && g >= acc + cq[qx]) { acc += cq[qx]; ++qx; }
;                 ent = u.seg[qx * 256 + (g - acc)]; } }
;         rowtab[tid] = ent;
.LBB0_707:
	s_or_b64 exec, exec, s[6:7]
	s_sub_i32 s8, s0, s16
	s_lshl_b32 s18, s8, 9
	v_add_u32_e32 v65, s18, v64
	s_movk_i32 s8, 0xff
	s_lshl_b64 s[6:7], s[4:5], 20
	v_cmp_lt_i32_e32 vcc, s8, v65
	s_waitcnt lgkmcnt(0)
	s_barrier
	s_and_saveexec_b64 s[8:9], vcc
	s_xor_b64 s[8:9], exec, s[8:9]
	s_cbranch_execz .LBB0_716
	v_add_u32_e32 v65, 0xffffff00, v65
	v_cmp_gt_i32_e32 vcc, s17, v65
	v_mov_b32_e32 v73, -1
	s_and_saveexec_b64 s[10:11], vcc
	s_cbranch_execz .LBB0_715
	v_mov_b32_e32 v124, 0x22800
	ds_read_b128 v[92:95], v124
	ds_read_b128 v[96:99], v124 offset:16
	ds_read_b128 v[100:103], v124 offset:32
	ds_read_b128 v[104:107], v124 offset:48
	ds_read_b128 v[108:111], v124 offset:64
	ds_read_b128 v[112:115], v124 offset:80
	ds_read_b128 v[116:119], v124 offset:96
	ds_read_b128 v[120:123], v124 offset:112
	v_mov_b32_e32 v75, 1
	v_mov_b32_e32 v73, v65
	s_waitcnt lgkmcnt(0)
	v_sub_u32_e32 v126, v65, v93
	v_cmp_le_i32_e32 vcc, v93, v65
	v_min_u32_e32 v73, v73, v126
	v_add_u32_e32 v125, v93, v94
	v_addc_co_u32_e32 v75, vcc, 0, v75, vcc
	v_sub_u32_e32 v126, v65, v125
	v_cmp_le_i32_e32 vcc, v125, v65
	v_min_u32_e32 v73, v73, v126
	v_add_u32_e32 v125, v125, v95
	v_addc_co_u32_e32 v75, vcc, 0, v75, vcc
	v_sub_u32_e32 v126, v65, v125
	v_cmp_le_i32_e32 vcc, v125, v65
	v_min_u32_e32 v73, v73, v126
	v_add_u32_e32 v125, v125, v96
	v_addc_co_u32_e32 v75, vcc, 0, v75, vcc
	v_sub_u32_e32 v126, v65, v125
	v_cmp_le_i32_e32 vcc, v125, v65
	v_min_u32_e32 v73, v73, v126
	v_add_u32_e32 v125, v125, v97
	v_addc_co_u32_e32 v75, vcc, 0, v75, vcc
	v_sub_u32_e32 v126, v65, v125
	v_cmp_le_i32_e32 vcc, v125, v65
	v_min_u32_e32 v73, v73, v126
	v_add_u32_e32 v125, v125, v98
	v_addc_co_u32_e32 v75, vcc, 0, v75, vcc
	v_sub_u32_e32 v126, v65, v125
	v_cmp_le_i32_e32 vcc, v125, v65
	v_min_u32_e32 v73, v73, v126
	v_add_u32_e32 v125, v125, v99
	v_addc_co_u32_e32 v75, vcc, 0, v75, vcc
	v_sub_u32_e32 v126, v65, v125
	v_cmp_le_i32_e32 vcc, v125, v65
	v_min_u32_e32 v73, v73, v126
	v_add_u32_e32 v125, v125, v100
	v_addc_co_u32_e32 v75, vcc, 0, v75, vcc
	v_sub_u32_e32 v126, v65, v125
	v_cmp_le_i32_e32 vcc, v125, v65
	v_min_u32_e32 v73, v73, v126
	v_add_u32_e32 v125, v125, v101
	v_addc_co_u32_e32 v75, vcc, 0, v75, vcc
	v_sub_u32_e32 v126, v65, v125
	v_cmp_le_i32_e32 vcc, v125, v65
	v_min_u32_e32 v73, v73, v126
	v_add_u32_e32 v125, v125, v102
	v_addc_co_u32_e32 v75, vcc, 0, v75, vcc
	v_sub_u32_e32 v126, v65, v125
	v_cmp_le_i32_e32 vcc, v125, v65
	v_min_u32_e32 v73, v73, v126
	v_add_u32_e32 v125, v125, v103
	v_addc_co_u32_e32 v75, vcc, 0, v75, vcc
	v_sub_u32_e32 v126, v65, v125
	v_cmp_le_i32_e32 vcc, v125, v65
	v_min_u32_e32 v73, v73, v126
	v_add_u32_e32 v125, v125, v104
	v_addc_co_u32_e32 v75, vcc, 0, v75, vcc
	v_sub_u32_e32 v126, v65, v125
	v_cmp_le_i32_e32 vcc, v125, v65
	v_min_u32_e32 v73, v73, v126
	v_add_u32_e32 v125, v125, v105
	v_addc_co_u32_e32 v75, vcc, 0, v75, vcc
	v_sub_u32_e32 v126, v65, v125
	v_cmp_le_i32_e32 vcc, v125, v65
	v_min_u32_e32 v73, v73, v126
	v_add_u32_e32 v125, v125, v106
	v_addc_co_u32_e32 v75, vcc, 0, v75, vcc
	v_sub_u32_e32 v126, v65, v125
	v_cmp_le_i32_e32 vcc, v125, v65
	v_min_u32_e32 v73, v73, v126
	v_add_u32_e32 v125, v125, v107
	v_addc_co_u32_e32 v75, vcc, 0, v75, vcc
	v_sub_u32_e32 v126, v65, v125
	v_cmp_le_i32_e32 vcc, v125, v65
	v_min_u32_e32 v73, v73, v126
	v_add_u32_e32 v125, v125, v108
	v_addc_co_u32_e32 v75, vcc, 0, v75, vcc
	v_sub_u32_e32 v126, v65, v125
	v_cmp_le_i32_e32 vcc, v125, v65
	v_min_u32_e32 v73, v73, v126
	v_add_u32_e32 v125, v125, v109
	v_addc_co_u32_e32 v75, vcc, 0, v75, vcc
	v_sub_u32_e32 v126, v65, v125
	v_cmp_le_i32_e32 vcc, v125, v65
	v_min_u32_e32 v73, v73, v126
	v_add_u32_e32 v125, v125, v110
	v_addc_co_u32_e32 v75, vcc, 0, v75, vcc
	v_sub_u32_e32 v126, v65, v125
	v_cmp_le_i32_e32 vcc, v125, v65
	v_min_u32_e32 v73, v73, v126
	v_add_u32_e32 v125, v125, v111
	v_addc_co_u32_e32 v75, vcc, 0, v75, vcc
	v_sub_u32_e32 v126, v65, v125
	v_cmp_le_i32_e32 vcc, v125, v65
	v_min_u32_e32 v73, v73, v126
	v_add_u32_e32 v125, v125, v112
	v_addc_co_u32_e32 v75, vcc, 0, v75, vcc
	v_sub_u32_e32 v126, v65, v125
	v_cmp_le_i32_e32 vcc, v125, v65
	v_min_u32_e32 v73, v73, v126
	v_add_u32_e32 v125, v125, v113
	v_addc_co_u32_e32 v75, vcc, 0, v75, vcc
	v_sub_u32_e32 v126, v65, v125
	v_cmp_le_i32_e32 vcc, v125, v65
	v_min_u32_e32 v73, v73, v126
	v_add_u32_e32 v125, v125, v114
	v_addc_co_u32_e32 v75, vcc, 0, v75, vcc
	v_sub_u32_e32 v126, v65, v125
	v_cmp_le_i32_e32 vcc, v125, v65
	v_min_u32_e32 v73, v73, v126
	v_add_u32_e32 v125, v125, v115
	v_addc_co_u32_e32 v75, vcc, 0, v75, vcc
	v_sub_u32_e32 v126, v65, v125
	v_cmp_le_i32_e32 vcc, v125, v65
	v_min_u32_e32 v73, v73, v126
	v_add_u32_e32 v125, v125, v116
	v_addc_co_u32_e32 v75, vcc, 0, v75, vcc
	v_sub_u32_e32 v126, v65, v125
	v_cmp_le_i32_e32 vcc, v125, v65
	v_min_u32_e32 v73, v73, v126
	v_add_u32_e32 v125, v125, v117
	v_addc_co_u32_e32 v75, vcc, 0, v75, vcc
	v_sub_u32_e32 v126, v65, v125
	v_cmp_le_i32_e32 vcc, v125, v65
	v_min_u32_e32 v73, v73, v126
	v_add_u32_e32 v125, v125, v118
	v_addc_co_u32_e32 v75, vcc, 0, v75, vcc
	v_sub_u32_e32 v126, v65, v125
	v_cmp_le_i32_e32 vcc, v125, v65
	v_min_u32_e32 v73, v73, v126
	v_add_u32_e32 v125, v125, v119
	v_addc_co_u32_e32 v75, vcc, 0, v75, vcc
	v_sub_u32_e32 v126, v65, v125
	v_cmp_le_i32_e32 vcc, v125, v65
	v_min_u32_e32 v73, v73, v126
	v_add_u32_e32 v125, v125, v120
	v_addc_co_u32_e32 v75, vcc, 0, v75, vcc
	v_sub_u32_e32 v126, v65, v125
	v_cmp_le_i32_e32 vcc, v125, v65
	v_min_u32_e32 v73, v73, v126
	v_add_u32_e32 v125, v125, v121
	v_addc_co_u32_e32 v75, vcc, 0, v75, vcc
	v_sub_u32_e32 v126, v65, v125
	v_cmp_le_i32_e32 vcc, v125, v65
	v_min_u32_e32 v73, v73, v126
	v_add_u32_e32 v125, v125, v122
	v_addc_co_u32_e32 v75, vcc, 0, v75, vcc
	v_sub_u32_e32 v126, v65, v125
	v_cmp_le_i32_e32 vcc, v125, v65
	v_min_u32_e32 v73, v73, v126
	s_nop 0
	v_addc_co_u32_e32 v75, vcc, 0, v75, vcc
	s_lshl_b64 s[2:3], s[2:3], 15
	v_readlane_b32 s1, v253, 27
	v_mov_b32_e32 v65, v73
	s_add_u32 s2, s1, s2
	v_readlane_b32 s1, v253, 28
	v_lshl_add_u32 v74, v75, 8, v65
	s_addc_u32 s3, s1, s3
	v_ashrrev_i32_e32 v75, 31, v74
	v_lshl_add_u64 v[74:75], v[74:75], 2, s[2:3]
	global_load_dword v73, v[74:75], off
